# rigorous early-invalidate barrier plus: the last three non-last arrivers of each XCD pre-flush the L2 (buffer_wbl2) while they poll, so the last arriver's release writeback finds little dirty data
# speedup vs baseline: 1.0041x; 1.0041x over previous
.LBB0_114:
	s_lshl_b32 s0, s0, 6
	s_add_i32 s6, s0, 0x500
	s_mov_b32 s7, 0
	s_lshl_b64 s[2:3], s[6:7], 2
	s_add_u32 s2, s36, s2
	s_addc_u32 s3, s37, s3
	v_mov_b32_e32 v1, 1
	v_mov_b64_e32 v[4:5], s[2:3]
	flat_atomic_add v1, v[4:5], v1 sc0
	v_cvt_f32_u32_e32 v3, v2
	v_sub_u32_e32 v4, 0, v2
	v_rcp_iflag_f32_e32 v3, v3
	s_nop 0
	v_mul_f32_e32 v3, 0x4f7ffffe, v3
	v_cvt_u32_f32_e32 v3, v3
	v_mul_lo_u32 v4, v4, v3
	v_mul_hi_u32 v4, v3, v4
	v_add_u32_e32 v3, v3, v4
	s_waitcnt vmcnt(0) lgkmcnt(0)
	v_mul_hi_u32 v3, v1, v3
	v_mul_lo_u32 v5, v3, v2
	v_add_u32_e32 v4, 1, v1
	v_sub_u32_e32 v1, v1, v5
	v_add_u32_e32 v6, 1, v3
	v_cmp_ge_u32_e32 vcc, v1, v2
	v_sub_u32_e32 v5, v1, v2
	s_nop 0
	v_cndmask_b32_e32 v3, v3, v6, vcc
	v_cndmask_b32_e32 v1, v1, v5, vcc
	v_add_u32_e32 v5, 1, v3
	v_cmp_ge_u32_e32 vcc, v1, v2
	s_nop 1
	v_cndmask_b32_e32 v1, v3, v5, vcc
	v_mad_u64_u32 v[2:3], s[2:3], v2, v1, v[2:3]
	v_cmp_ne_u32_e32 vcc, v4, v2
	s_and_saveexec_b64 s[2:3], vcc
	s_xor_b64 s[4:5], exec, s[2:3]
	s_cbranch_execz .LBB0_127
	v_sub_u32_e32 v18, v2, v4
	v_cmp_gt_u32_e32 vcc, 4, v18
	s_cbranch_vccz .Lnowb_0
	buffer_wbl2 sc1
.Lnowb_0:
	buffer_inv sc1
	s_add_i32 s6, s0, 0x900
	s_lshl_b64 s[2:3], s[6:7], 2
	s_add_u32 s8, s36, s2
	s_addc_u32 s9, s37, s3
	v_mov_b64_e32 v[2:3], s[8:9]
	flat_load_dword v0, v[2:3] sc1
	s_waitcnt vmcnt(0) lgkmcnt(0)
	v_cmp_eq_u32_e32 vcc, v0, v1
	s_and_saveexec_b64 s[6:7], vcc
	s_cbranch_execz .LBB0_126
	s_mov_b32 s1, 1
	s_mov_b64 s[10:11], 0
	s_branch .LBB0_118

.LBB0_245:
	s_lshl_b32 s22, s34, 6
	s_add_i32 s36, s22, 0x500
	s_lshl_b64 s[0:1], s[36:37], 2
	s_add_u32 s0, s62, s0
	s_addc_u32 s1, s63, s1
	v_mov_b64_e32 v[4:5], s[0:1]
	flat_atomic_add v3, v[4:5], v205 sc0
	v_cvt_f32_u32_e32 v1, v2
	v_sub_u32_e32 v4, 0, v2
	v_rcp_iflag_f32_e32 v1, v1
	s_nop 0
	v_mul_f32_e32 v1, 0x4f7ffffe, v1
	v_cvt_u32_f32_e32 v1, v1
	v_mul_lo_u32 v4, v4, v1
	v_mul_hi_u32 v4, v1, v4
	v_add_u32_e32 v1, v1, v4
	s_waitcnt vmcnt(0) lgkmcnt(0)
	v_mul_hi_u32 v1, v3, v1
	v_mul_lo_u32 v4, v1, v2
	v_sub_u32_e32 v4, v3, v4
	v_cmp_ge_u32_e32 vcc, v4, v2
	v_add_u32_e32 v5, 1, v1
	s_nop 0
	v_cndmask_b32_e32 v1, v1, v5, vcc
	v_sub_u32_e32 v5, v4, v2
	v_cndmask_b32_e32 v4, v4, v5, vcc
	v_cmp_ge_u32_e32 vcc, v4, v2
	v_add_u32_e32 v4, 1, v1
	s_nop 0
	v_cndmask_b32_e32 v1, v1, v4, vcc
	v_add_u32_e32 v4, 1, v3
	v_mad_u64_u32 v[2:3], s[0:1], v2, v1, v[2:3]
	v_cmp_ne_u32_e32 vcc, v4, v2
	s_and_saveexec_b64 s[0:1], vcc
	s_xor_b64 s[0:1], exec, s[0:1]
	s_cbranch_execz .LBB0_258
	v_sub_u32_e32 v18, v2, v4
	v_cmp_gt_u32_e32 vcc, 4, v18
	s_cbranch_vccz .Lnowb_1
	buffer_wbl2 sc1
.Lnowb_1:
	buffer_inv sc1
	s_add_i32 s36, s22, 0x900
	s_lshl_b64 s[4:5], s[36:37], 2
	s_add_u32 s6, s62, s4
	s_addc_u32 s7, s63, s5
	v_mov_b64_e32 v[2:3], s[6:7]
	flat_load_dword v0, v[2:3] sc1
	s_waitcnt vmcnt(0) lgkmcnt(0)
	v_cmp_eq_u32_e32 vcc, v0, v1
	s_and_saveexec_b64 s[4:5], vcc
	s_cbranch_execz .LBB0_257
	s_mov_b32 s2, 1
	s_mov_b64 s[8:9], 0
	s_branch .LBB0_249

.LBB0_1206:
	s_lshl_b32 s22, s34, 6
	s_add_i32 s36, s22, 0x500
	s_lshl_b64 s[0:1], s[36:37], 2
	s_add_u32 s0, s60, s0
	s_addc_u32 s1, s61, s1
	v_mov_b64_e32 v[4:5], s[0:1]
	flat_atomic_add v3, v[4:5], v205 sc0
	v_cvt_f32_u32_e32 v1, v2
	v_sub_u32_e32 v4, 0, v2
	v_rcp_iflag_f32_e32 v1, v1
	s_nop 0
	v_mul_f32_e32 v1, 0x4f7ffffe, v1
	v_cvt_u32_f32_e32 v1, v1
	v_mul_lo_u32 v4, v4, v1
	v_mul_hi_u32 v4, v1, v4
	v_add_u32_e32 v1, v1, v4
	s_waitcnt vmcnt(0) lgkmcnt(0)
	v_mul_hi_u32 v1, v3, v1
	v_mul_lo_u32 v4, v1, v2
	v_sub_u32_e32 v4, v3, v4
	v_cmp_ge_u32_e32 vcc, v4, v2
	v_add_u32_e32 v5, 1, v1
	s_nop 0
	v_cndmask_b32_e32 v1, v1, v5, vcc
	v_sub_u32_e32 v5, v4, v2
	v_cndmask_b32_e32 v4, v4, v5, vcc
	v_cmp_ge_u32_e32 vcc, v4, v2
	v_add_u32_e32 v4, 1, v1
	s_nop 0
	v_cndmask_b32_e32 v1, v1, v4, vcc
	v_add_u32_e32 v4, 1, v3
	v_mad_u64_u32 v[2:3], s[0:1], v2, v1, v[2:3]
	v_cmp_ne_u32_e32 vcc, v4, v2
	s_and_saveexec_b64 s[0:1], vcc
	s_xor_b64 s[0:1], exec, s[0:1]
	s_cbranch_execz .LBB0_1219
	v_sub_u32_e32 v18, v2, v4
	v_cmp_gt_u32_e32 vcc, 4, v18
	s_cbranch_vccz .Lnowb_10
	buffer_wbl2 sc1
.Lnowb_10:
	buffer_inv sc1
	s_add_i32 s36, s22, 0x900
	s_lshl_b64 s[4:5], s[36:37], 2
	s_add_u32 s6, s60, s4
	s_addc_u32 s7, s61, s5
	v_mov_b64_e32 v[2:3], s[6:7]
	flat_load_dword v0, v[2:3] sc1
	s_waitcnt vmcnt(0) lgkmcnt(0)
	v_cmp_eq_u32_e32 vcc, v0, v1
	s_and_saveexec_b64 s[4:5], vcc
	s_cbranch_execz .LBB0_1218
	s_mov_b32 s2, 1
	s_mov_b64 s[8:9], 0
	s_branch .LBB0_1210
